# same as previous but the static priority raise goes to waves 0-3 (the leading half) instead of waves 4-7
# baseline (speedup 1.0000x reference)
.LBB0_417:
	s_ashr_i32 s25, s24, 31
	s_lshl_b64 s[36:37], s[24:25], 21
	s_add_u32 s36, s48, s36
	s_addc_u32 s37, s49, s37
	s_and_b64 s[44:45], s[2:3], exec
	s_cselect_b32 s5, s37, s35
	s_cselect_b32 s7, s36, s34
	s_ashr_i32 s15, s14, 31
	s_lshl_b64 s[44:45], s[14:15], 21
	v_readlane_b32 s16, v254, 42
	v_readlane_b32 s17, v254, 43
	s_add_u32 s64, s16, s44
	s_addc_u32 s65, s17, s45
	s_and_b64 s[44:45], s[2:3], exec
	s_cselect_b32 s15, s65, s43
	s_cselect_b32 s25, s64, s42
	s_add_u32 s34, s34, 0x100080
	s_addc_u32 s35, s35, 0
	s_add_u32 s63, s42, 0x100
	v_mov_b32_e32 v2, 0
	s_addc_u32 s66, s43, 0
	s_mov_b32 s67, -2
	v_mov_b32_e32 v3, v2
	v_mov_b32_e32 v4, v2
	v_mov_b32_e32 v5, v2
	v_mov_b32_e32 v6, v2
	v_mov_b32_e32 v7, v2
	v_mov_b32_e32 v8, v2
	v_mov_b32_e32 v9, v2
	v_mov_b32_e32 v18, v2
	v_mov_b32_e32 v19, v2
	v_mov_b32_e32 v20, v2
	v_mov_b32_e32 v21, v2
	v_mov_b32_e32 v22, v2
	v_mov_b32_e32 v23, v2
	v_mov_b32_e32 v24, v2
	v_mov_b32_e32 v25, v2
	v_mov_b32_e32 v34, v2
	v_mov_b32_e32 v35, v2
	v_mov_b32_e32 v36, v2
	v_mov_b32_e32 v37, v2
	v_mov_b32_e32 v38, v2
	v_mov_b32_e32 v39, v2
	v_mov_b32_e32 v40, v2
	v_mov_b32_e32 v41, v2
	v_mov_b32_e32 v50, v2
	v_mov_b32_e32 v51, v2
	v_mov_b32_e32 v52, v2
	v_mov_b32_e32 v53, v2
	v_mov_b32_e32 v54, v2
	v_mov_b32_e32 v55, v2
	v_mov_b32_e32 v56, v2
	v_mov_b32_e32 v57, v2
	v_mov_b32_e32 v10, v2
	v_mov_b32_e32 v11, v2
	v_mov_b32_e32 v12, v2
	v_mov_b32_e32 v13, v2
	v_mov_b32_e32 v14, v2
	v_mov_b32_e32 v15, v2
	v_mov_b32_e32 v16, v2
	v_mov_b32_e32 v17, v2
	v_mov_b32_e32 v26, v2
	v_mov_b32_e32 v27, v2
	v_mov_b32_e32 v28, v2
	v_mov_b32_e32 v29, v2
	v_mov_b32_e32 v30, v2
	v_mov_b32_e32 v31, v2
	v_mov_b32_e32 v32, v2
	v_mov_b32_e32 v33, v2
	v_mov_b32_e32 v42, v2
	v_mov_b32_e32 v43, v2
	v_mov_b32_e32 v44, v2
	v_mov_b32_e32 v45, v2
	v_mov_b32_e32 v46, v2
	v_mov_b32_e32 v47, v2
	v_mov_b32_e32 v48, v2
	v_mov_b32_e32 v49, v2
	v_mov_b32_e32 v58, v2
	v_mov_b32_e32 v59, v2
	v_mov_b32_e32 v60, v2
	v_mov_b32_e32 v61, v2
	v_mov_b32_e32 v62, v2
	v_mov_b32_e32 v63, v2
	v_mov_b32_e32 v64, v2
	v_mov_b32_e32 v65, v2
	v_mov_b32_e32 v66, v2
	v_mov_b32_e32 v67, v2
	v_mov_b32_e32 v68, v2
	v_mov_b32_e32 v69, v2
	v_mov_b32_e32 v70, v2
	v_mov_b32_e32 v71, v2
	v_mov_b32_e32 v72, v2
	v_mov_b32_e32 v73, v2
	v_mov_b32_e32 v82, v2
	v_mov_b32_e32 v83, v2
	v_mov_b32_e32 v84, v2
	v_mov_b32_e32 v85, v2
	v_mov_b32_e32 v86, v2
	v_mov_b32_e32 v87, v2
	v_mov_b32_e32 v88, v2
	v_mov_b32_e32 v89, v2
	v_mov_b32_e32 v98, v2
	v_mov_b32_e32 v99, v2
	v_mov_b32_e32 v100, v2
	v_mov_b32_e32 v101, v2
	v_mov_b32_e32 v102, v2
	v_mov_b32_e32 v103, v2
	v_mov_b32_e32 v104, v2
	v_mov_b32_e32 v105, v2
	v_mov_b32_e32 v114, v2
	v_mov_b32_e32 v115, v2
	v_mov_b32_e32 v116, v2
	v_mov_b32_e32 v117, v2
	v_mov_b32_e32 v118, v2
	v_mov_b32_e32 v119, v2
	v_mov_b32_e32 v120, v2
	v_mov_b32_e32 v121, v2
	v_mov_b32_e32 v74, v2
	v_mov_b32_e32 v75, v2
	v_mov_b32_e32 v76, v2
	v_mov_b32_e32 v77, v2
	v_mov_b32_e32 v78, v2
	v_mov_b32_e32 v79, v2
	v_mov_b32_e32 v80, v2
	v_mov_b32_e32 v81, v2
	v_mov_b32_e32 v90, v2
	v_mov_b32_e32 v91, v2
	v_mov_b32_e32 v92, v2
	v_mov_b32_e32 v93, v2
	v_mov_b32_e32 v94, v2
	v_mov_b32_e32 v95, v2
	v_mov_b32_e32 v96, v2
	v_mov_b32_e32 v97, v2
	v_mov_b32_e32 v106, v2
	v_mov_b32_e32 v107, v2
	v_mov_b32_e32 v108, v2
	v_mov_b32_e32 v109, v2
	v_mov_b32_e32 v110, v2
	v_mov_b32_e32 v111, v2
	v_mov_b32_e32 v112, v2
	v_mov_b32_e32 v113, v2
	v_mov_b32_e32 v122, v2
	v_mov_b32_e32 v123, v2
	v_mov_b32_e32 v124, v2
	v_mov_b32_e32 v125, v2
	v_mov_b32_e32 v126, v2
	v_mov_b32_e32 v127, v2
	v_mov_b32_e32 v128, v2
	v_mov_b32_e32 v129, v2
	v_readfirstlane_b32 s38, v0
	s_nop 3
	s_lshr_b32 s38, s38, 6
	s_cmp_ge_u32 s38, 4
	s_cbranch_scc1 .Lprio_P2a
	s_setprio 1

.LBB0_546:
	s_ashr_i32 s67, s66, 31
	s_lshl_b64 s[44:45], s[66:67], 20
	s_add_u32 s84, s96, s44
	s_addc_u32 s85, s97, s45
	s_and_b64 s[44:45], s[2:3], exec
	s_cselect_b32 s5, s85, s35
	s_cselect_b32 s7, s84, s34
	s_ashr_i32 s65, s64, 31
	s_lshl_b64 s[44:45], s[64:65], 20
	s_add_u32 s86, s33, s44
	s_addc_u32 s87, s46, s45
	s_and_b64 s[44:45], s[2:3], exec
	s_cselect_b32 s8, s87, s43
	s_cselect_b32 s65, s86, s42
	s_add_u32 s34, s34, 0x80080
	s_addc_u32 s35, s35, 0
	s_add_u32 s67, s42, 0x100
	v_mov_b32_e32 v2, 0
	s_addc_u32 s73, s43, 0
	s_mov_b32 s74, -2
	v_mov_b32_e32 v3, v2
	v_mov_b32_e32 v4, v2
	v_mov_b32_e32 v5, v2
	v_mov_b32_e32 v6, v2
	v_mov_b32_e32 v7, v2
	v_mov_b32_e32 v8, v2
	v_mov_b32_e32 v9, v2
	v_mov_b32_e32 v18, v2
	v_mov_b32_e32 v19, v2
	v_mov_b32_e32 v20, v2
	v_mov_b32_e32 v21, v2
	v_mov_b32_e32 v22, v2
	v_mov_b32_e32 v23, v2
	v_mov_b32_e32 v24, v2
	v_mov_b32_e32 v25, v2
	v_mov_b32_e32 v50, v2
	v_mov_b32_e32 v51, v2
	v_mov_b32_e32 v52, v2
	v_mov_b32_e32 v53, v2
	v_mov_b32_e32 v54, v2
	v_mov_b32_e32 v55, v2
	v_mov_b32_e32 v56, v2
	v_mov_b32_e32 v57, v2
	v_mov_b32_e32 v66, v2
	v_mov_b32_e32 v67, v2
	v_mov_b32_e32 v68, v2
	v_mov_b32_e32 v69, v2
	v_mov_b32_e32 v70, v2
	v_mov_b32_e32 v71, v2
	v_mov_b32_e32 v72, v2
	v_mov_b32_e32 v73, v2
	v_mov_b32_e32 v10, v2
	v_mov_b32_e32 v11, v2
	v_mov_b32_e32 v12, v2
	v_mov_b32_e32 v13, v2
	v_mov_b32_e32 v14, v2
	v_mov_b32_e32 v15, v2
	v_mov_b32_e32 v16, v2
	v_mov_b32_e32 v17, v2
	v_mov_b32_e32 v34, v2
	v_mov_b32_e32 v35, v2
	v_mov_b32_e32 v36, v2
	v_mov_b32_e32 v37, v2
	v_mov_b32_e32 v38, v2
	v_mov_b32_e32 v39, v2
	v_mov_b32_e32 v40, v2
	v_mov_b32_e32 v41, v2
	v_mov_b32_e32 v58, v2
	v_mov_b32_e32 v59, v2
	v_mov_b32_e32 v60, v2
	v_mov_b32_e32 v61, v2
	v_mov_b32_e32 v62, v2
	v_mov_b32_e32 v63, v2
	v_mov_b32_e32 v64, v2
	v_mov_b32_e32 v65, v2
	v_mov_b32_e32 v74, v2
	v_mov_b32_e32 v75, v2
	v_mov_b32_e32 v76, v2
	v_mov_b32_e32 v77, v2
	v_mov_b32_e32 v78, v2
	v_mov_b32_e32 v79, v2
	v_mov_b32_e32 v80, v2
	v_mov_b32_e32 v81, v2
	v_mov_b32_e32 v82, v2
	v_mov_b32_e32 v83, v2
	v_mov_b32_e32 v84, v2
	v_mov_b32_e32 v85, v2
	v_mov_b32_e32 v86, v2
	v_mov_b32_e32 v87, v2
	v_mov_b32_e32 v88, v2
	v_mov_b32_e32 v89, v2
	v_mov_b32_e32 v98, v2
	v_mov_b32_e32 v99, v2
	v_mov_b32_e32 v100, v2
	v_mov_b32_e32 v101, v2
	v_mov_b32_e32 v102, v2
	v_mov_b32_e32 v103, v2
	v_mov_b32_e32 v104, v2
	v_mov_b32_e32 v105, v2
	v_mov_b32_e32 v114, v2
	v_mov_b32_e32 v115, v2
	v_mov_b32_e32 v116, v2
	v_mov_b32_e32 v117, v2
	v_mov_b32_e32 v118, v2
	v_mov_b32_e32 v119, v2
	v_mov_b32_e32 v120, v2
	v_mov_b32_e32 v121, v2
	v_mov_b32_e32 v130, v2
	v_mov_b32_e32 v131, v2
	v_mov_b32_e32 v132, v2
	v_mov_b32_e32 v133, v2
	v_mov_b32_e32 v134, v2
	v_mov_b32_e32 v135, v2
	v_mov_b32_e32 v136, v2
	v_mov_b32_e32 v137, v2
	v_mov_b32_e32 v90, v2
	v_mov_b32_e32 v91, v2
	v_mov_b32_e32 v92, v2
	v_mov_b32_e32 v93, v2
	v_mov_b32_e32 v94, v2
	v_mov_b32_e32 v95, v2
	v_mov_b32_e32 v96, v2
	v_mov_b32_e32 v97, v2
	v_mov_b32_e32 v106, v2
	v_mov_b32_e32 v107, v2
	v_mov_b32_e32 v108, v2
	v_mov_b32_e32 v109, v2
	v_mov_b32_e32 v110, v2
	v_mov_b32_e32 v111, v2
	v_mov_b32_e32 v112, v2
	v_mov_b32_e32 v113, v2
	v_mov_b32_e32 v122, v2
	v_mov_b32_e32 v123, v2
	v_mov_b32_e32 v124, v2
	v_mov_b32_e32 v125, v2
	v_mov_b32_e32 v126, v2
	v_mov_b32_e32 v127, v2
	v_mov_b32_e32 v128, v2
	v_mov_b32_e32 v129, v2
	v_mov_b32_e32 v138, v2
	v_mov_b32_e32 v139, v2
	v_mov_b32_e32 v140, v2
	v_mov_b32_e32 v141, v2
	v_mov_b32_e32 v142, v2
	v_mov_b32_e32 v143, v2
	v_mov_b32_e32 v144, v2
	v_mov_b32_e32 v145, v2
	v_readfirstlane_b32 s38, v0
	s_nop 3
	s_lshr_b32 s38, s38, 6
	s_cmp_ge_u32 s38, 4
	s_cbranch_scc1 .Lprio_P2b
	s_setprio 1

.LBB0_672:
	s_ashr_i32 s25, s24, 31
	s_lshl_b64 s[36:37], s[24:25], 20
	s_add_u32 s36, s50, s36
	s_addc_u32 s37, s51, s37
	s_and_b64 s[46:47], s[2:3], exec
	s_cselect_b32 s25, s37, s45
	s_cselect_b32 s73, s36, s44
	s_ashr_i32 s15, s14, 31
	s_lshl_b64 s[46:47], s[14:15], 20
	s_add_u32 s64, s96, s46
	s_addc_u32 s65, s97, s47
	s_and_b64 s[46:47], s[2:3], exec
	s_cselect_b32 s15, s65, s43
	s_cselect_b32 s74, s64, s42
	s_add_u32 s44, s44, 0x80080
	s_addc_u32 s45, s45, 0
	s_add_u32 s75, s42, 0x100
	v_mov_b32_e32 v2, 0
	s_addc_u32 s76, s43, 0
	s_mov_b32 s77, -2
	v_mov_b32_e32 v3, v2
	v_mov_b32_e32 v4, v2
	v_mov_b32_e32 v5, v2
	v_mov_b32_e32 v6, v2
	v_mov_b32_e32 v7, v2
	v_mov_b32_e32 v8, v2
	v_mov_b32_e32 v9, v2
	v_mov_b32_e32 v18, v2
	v_mov_b32_e32 v19, v2
	v_mov_b32_e32 v20, v2
	v_mov_b32_e32 v21, v2
	v_mov_b32_e32 v22, v2
	v_mov_b32_e32 v23, v2
	v_mov_b32_e32 v24, v2
	v_mov_b32_e32 v25, v2
	v_mov_b32_e32 v34, v2
	v_mov_b32_e32 v35, v2
	v_mov_b32_e32 v36, v2
	v_mov_b32_e32 v37, v2
	v_mov_b32_e32 v38, v2
	v_mov_b32_e32 v39, v2
	v_mov_b32_e32 v40, v2
	v_mov_b32_e32 v41, v2
	v_mov_b32_e32 v50, v2
	v_mov_b32_e32 v51, v2
	v_mov_b32_e32 v52, v2
	v_mov_b32_e32 v53, v2
	v_mov_b32_e32 v54, v2
	v_mov_b32_e32 v55, v2
	v_mov_b32_e32 v56, v2
	v_mov_b32_e32 v57, v2
	v_mov_b32_e32 v10, v2
	v_mov_b32_e32 v11, v2
	v_mov_b32_e32 v12, v2
	v_mov_b32_e32 v13, v2
	v_mov_b32_e32 v14, v2
	v_mov_b32_e32 v15, v2
	v_mov_b32_e32 v16, v2
	v_mov_b32_e32 v17, v2
	v_mov_b32_e32 v26, v2
	v_mov_b32_e32 v27, v2
	v_mov_b32_e32 v28, v2
	v_mov_b32_e32 v29, v2
	v_mov_b32_e32 v30, v2
	v_mov_b32_e32 v31, v2
	v_mov_b32_e32 v32, v2
	v_mov_b32_e32 v33, v2
	v_mov_b32_e32 v42, v2
	v_mov_b32_e32 v43, v2
	v_mov_b32_e32 v44, v2
	v_mov_b32_e32 v45, v2
	v_mov_b32_e32 v46, v2
	v_mov_b32_e32 v47, v2
	v_mov_b32_e32 v48, v2
	v_mov_b32_e32 v49, v2
	v_mov_b32_e32 v58, v2
	v_mov_b32_e32 v59, v2
	v_mov_b32_e32 v60, v2
	v_mov_b32_e32 v61, v2
	v_mov_b32_e32 v62, v2
	v_mov_b32_e32 v63, v2
	v_mov_b32_e32 v64, v2
	v_mov_b32_e32 v65, v2
	v_mov_b32_e32 v66, v2
	v_mov_b32_e32 v67, v2
	v_mov_b32_e32 v68, v2
	v_mov_b32_e32 v69, v2
	v_mov_b32_e32 v70, v2
	v_mov_b32_e32 v71, v2
	v_mov_b32_e32 v72, v2
	v_mov_b32_e32 v73, v2
	v_mov_b32_e32 v82, v2
	v_mov_b32_e32 v83, v2
	v_mov_b32_e32 v84, v2
	v_mov_b32_e32 v85, v2
	v_mov_b32_e32 v86, v2
	v_mov_b32_e32 v87, v2
	v_mov_b32_e32 v88, v2
	v_mov_b32_e32 v89, v2
	v_mov_b32_e32 v98, v2
	v_mov_b32_e32 v99, v2
	v_mov_b32_e32 v100, v2
	v_mov_b32_e32 v101, v2
	v_mov_b32_e32 v102, v2
	v_mov_b32_e32 v103, v2
	v_mov_b32_e32 v104, v2
	v_mov_b32_e32 v105, v2
	v_mov_b32_e32 v114, v2
	v_mov_b32_e32 v115, v2
	v_mov_b32_e32 v116, v2
	v_mov_b32_e32 v117, v2
	v_mov_b32_e32 v118, v2
	v_mov_b32_e32 v119, v2
	v_mov_b32_e32 v120, v2
	v_mov_b32_e32 v121, v2
	v_mov_b32_e32 v74, v2
	v_mov_b32_e32 v75, v2
	v_mov_b32_e32 v76, v2
	v_mov_b32_e32 v77, v2
	v_mov_b32_e32 v78, v2
	v_mov_b32_e32 v79, v2
	v_mov_b32_e32 v80, v2
	v_mov_b32_e32 v81, v2
	v_mov_b32_e32 v90, v2
	v_mov_b32_e32 v91, v2
	v_mov_b32_e32 v92, v2
	v_mov_b32_e32 v93, v2
	v_mov_b32_e32 v94, v2
	v_mov_b32_e32 v95, v2
	v_mov_b32_e32 v96, v2
	v_mov_b32_e32 v97, v2
	v_mov_b32_e32 v106, v2
	v_mov_b32_e32 v107, v2
	v_mov_b32_e32 v108, v2
	v_mov_b32_e32 v109, v2
	v_mov_b32_e32 v110, v2
	v_mov_b32_e32 v111, v2
	v_mov_b32_e32 v112, v2
	v_mov_b32_e32 v113, v2
	v_mov_b32_e32 v138, v2
	v_mov_b32_e32 v139, v2
	v_mov_b32_e32 v140, v2
	v_mov_b32_e32 v141, v2
	v_mov_b32_e32 v142, v2
	v_mov_b32_e32 v143, v2
	v_mov_b32_e32 v144, v2
	v_mov_b32_e32 v145, v2
	v_readfirstlane_b32 s38, v0
	s_nop 3
	s_lshr_b32 s38, s38, 6
	s_cmp_ge_u32 s38, 4
	s_cbranch_scc1 .Lprio_P2c
	s_setprio 1

.LBB0_1488:
	s_ashr_i32 s17, s16, 31
	s_lshl_b64 s[18:19], s[16:17], 20
	s_add_u32 s18, s62, s18
	s_addc_u32 s19, s63, s19
	s_and_b64 s[20:21], s[2:3], exec
	s_cselect_b32 s17, s19, s25
	s_cselect_b32 s49, s18, s24
	s_ashr_i32 s15, s14, 31
	s_lshl_b64 s[20:21], s[14:15], 20
	s_add_u32 s20, s31, s20
	s_addc_u32 s21, s33, s21
	s_and_b64 s[28:29], s[2:3], exec
	s_cselect_b32 s15, s21, s27
	s_cselect_b32 s50, s20, s26
	s_add_u32 s24, s24, 0x80080
	s_addc_u32 s25, s25, 0
	s_add_u32 s51, s26, 0x100
	v_mov_b32_e32 v2, 0
	s_addc_u32 s52, s27, 0
	s_mov_b32 s53, -2
	v_mov_b32_e32 v3, v2
	v_mov_b32_e32 v4, v2
	v_mov_b32_e32 v5, v2
	v_mov_b32_e32 v6, v2
	v_mov_b32_e32 v7, v2
	v_mov_b32_e32 v8, v2
	v_mov_b32_e32 v9, v2
	v_mov_b32_e32 v18, v2
	v_mov_b32_e32 v19, v2
	v_mov_b32_e32 v20, v2
	v_mov_b32_e32 v21, v2
	v_mov_b32_e32 v22, v2
	v_mov_b32_e32 v23, v2
	v_mov_b32_e32 v24, v2
	v_mov_b32_e32 v25, v2
	v_mov_b32_e32 v34, v2
	v_mov_b32_e32 v35, v2
	v_mov_b32_e32 v36, v2
	v_mov_b32_e32 v37, v2
	v_mov_b32_e32 v38, v2
	v_mov_b32_e32 v39, v2
	v_mov_b32_e32 v40, v2
	v_mov_b32_e32 v41, v2
	v_mov_b32_e32 v50, v2
	v_mov_b32_e32 v51, v2
	v_mov_b32_e32 v52, v2
	v_mov_b32_e32 v53, v2
	v_mov_b32_e32 v54, v2
	v_mov_b32_e32 v55, v2
	v_mov_b32_e32 v56, v2
	v_mov_b32_e32 v57, v2
	v_mov_b32_e32 v10, v2
	v_mov_b32_e32 v11, v2
	v_mov_b32_e32 v12, v2
	v_mov_b32_e32 v13, v2
	v_mov_b32_e32 v14, v2
	v_mov_b32_e32 v15, v2
	v_mov_b32_e32 v16, v2
	v_mov_b32_e32 v17, v2
	v_mov_b32_e32 v26, v2
	v_mov_b32_e32 v27, v2
	v_mov_b32_e32 v28, v2
	v_mov_b32_e32 v29, v2
	v_mov_b32_e32 v30, v2
	v_mov_b32_e32 v31, v2
	v_mov_b32_e32 v32, v2
	v_mov_b32_e32 v33, v2
	v_mov_b32_e32 v42, v2
	v_mov_b32_e32 v43, v2
	v_mov_b32_e32 v44, v2
	v_mov_b32_e32 v45, v2
	v_mov_b32_e32 v46, v2
	v_mov_b32_e32 v47, v2
	v_mov_b32_e32 v48, v2
	v_mov_b32_e32 v49, v2
	v_mov_b32_e32 v58, v2
	v_mov_b32_e32 v59, v2
	v_mov_b32_e32 v60, v2
	v_mov_b32_e32 v61, v2
	v_mov_b32_e32 v62, v2
	v_mov_b32_e32 v63, v2
	v_mov_b32_e32 v64, v2
	v_mov_b32_e32 v65, v2
	v_mov_b32_e32 v66, v2
	v_mov_b32_e32 v67, v2
	v_mov_b32_e32 v68, v2
	v_mov_b32_e32 v69, v2
	v_mov_b32_e32 v70, v2
	v_mov_b32_e32 v71, v2
	v_mov_b32_e32 v72, v2
	v_mov_b32_e32 v73, v2
	v_mov_b32_e32 v82, v2
	v_mov_b32_e32 v83, v2
	v_mov_b32_e32 v84, v2
	v_mov_b32_e32 v85, v2
	v_mov_b32_e32 v86, v2
	v_mov_b32_e32 v87, v2
	v_mov_b32_e32 v88, v2
	v_mov_b32_e32 v89, v2
	v_mov_b32_e32 v98, v2
	v_mov_b32_e32 v99, v2
	v_mov_b32_e32 v100, v2
	v_mov_b32_e32 v101, v2
	v_mov_b32_e32 v102, v2
	v_mov_b32_e32 v103, v2
	v_mov_b32_e32 v104, v2
	v_mov_b32_e32 v105, v2
	v_mov_b32_e32 v114, v2
	v_mov_b32_e32 v115, v2
	v_mov_b32_e32 v116, v2
	v_mov_b32_e32 v117, v2
	v_mov_b32_e32 v118, v2
	v_mov_b32_e32 v119, v2
	v_mov_b32_e32 v120, v2
	v_mov_b32_e32 v121, v2
	v_mov_b32_e32 v74, v2
	v_mov_b32_e32 v75, v2
	v_mov_b32_e32 v76, v2
	v_mov_b32_e32 v77, v2
	v_mov_b32_e32 v78, v2
	v_mov_b32_e32 v79, v2
	v_mov_b32_e32 v80, v2
	v_mov_b32_e32 v81, v2
	v_mov_b32_e32 v90, v2
	v_mov_b32_e32 v91, v2
	v_mov_b32_e32 v92, v2
	v_mov_b32_e32 v93, v2
	v_mov_b32_e32 v94, v2
	v_mov_b32_e32 v95, v2
	v_mov_b32_e32 v96, v2
	v_mov_b32_e32 v97, v2
	v_mov_b32_e32 v106, v2
	v_mov_b32_e32 v107, v2
	v_mov_b32_e32 v108, v2
	v_mov_b32_e32 v109, v2
	v_mov_b32_e32 v110, v2
	v_mov_b32_e32 v111, v2
	v_mov_b32_e32 v112, v2
	v_mov_b32_e32 v113, v2
	v_mov_b32_e32 v138, v2
	v_mov_b32_e32 v139, v2
	v_mov_b32_e32 v140, v2
	v_mov_b32_e32 v141, v2
	v_mov_b32_e32 v142, v2
	v_mov_b32_e32 v143, v2
	v_mov_b32_e32 v144, v2
	v_mov_b32_e32 v145, v2
	v_readfirstlane_b32 s26, v0
	s_nop 3
	s_lshr_b32 s26, s26, 6
	s_cmp_ge_u32 s26, 4
	s_cbranch_scc1 .Lprio_P6
	s_setprio 1

.LBB0_1648:
	s_ashr_i32 s29, s28, 31
	s_lshl_b64 s[30:31], s[28:29], 20
	v_readlane_b32 s36, v254, 42
	v_readlane_b32 s37, v254, 43
	s_add_u32 s30, s36, s30
	s_addc_u32 s31, s37, s31
	s_and_b64 s[36:37], s[2:3], exec
	s_cselect_b32 s1, s31, s35
	s_cselect_b32 s29, s30, s34
	s_ashr_i32 s27, s26, 31
	s_lshl_b64 s[36:37], s[26:27], 20
	s_add_u32 s36, s33, s36
	s_addc_u32 s37, s48, s37
	s_and_b64 s[38:39], s[2:3], exec
	s_cselect_b32 s27, s37, s43
	s_cselect_b32 s41, s36, s42
	s_add_u32 s34, s34, 0x80080
	s_addc_u32 s35, s35, 0
	s_add_u32 s46, s42, 0x100
	v_mov_b32_e32 v98, 0
	s_addc_u32 s47, s43, 0
	s_mov_b32 s77, -2
	v_mov_b32_e32 v99, v98
	v_mov_b32_e32 v100, v98
	v_mov_b32_e32 v101, v98
	v_mov_b32_e32 v102, v98
	v_mov_b32_e32 v103, v98
	v_mov_b32_e32 v104, v98
	v_mov_b32_e32 v105, v98
	v_mov_b32_e32 v50, v98
	v_mov_b32_e32 v51, v98
	v_mov_b32_e32 v52, v98
	v_mov_b32_e32 v53, v98
	v_mov_b32_e32 v74, v98
	v_mov_b32_e32 v75, v98
	v_mov_b32_e32 v76, v98
	v_mov_b32_e32 v77, v98
	v_mov_b32_e32 v58, v98
	v_mov_b32_e32 v59, v98
	v_mov_b32_e32 v60, v98
	v_mov_b32_e32 v61, v98
	v_mov_b32_e32 v82, v98
	v_mov_b32_e32 v83, v98
	v_mov_b32_e32 v84, v98
	v_mov_b32_e32 v85, v98
	v_mov_b32_e32 v66, v98
	v_mov_b32_e32 v67, v98
	v_mov_b32_e32 v68, v98
	v_mov_b32_e32 v69, v98
	v_mov_b32_e32 v90, v98
	v_mov_b32_e32 v91, v98
	v_mov_b32_e32 v92, v98
	v_mov_b32_e32 v93, v98
	v_mov_b32_e32 v106, v98
	v_mov_b32_e32 v107, v98
	v_mov_b32_e32 v108, v98
	v_mov_b32_e32 v109, v98
	v_mov_b32_e32 v110, v98
	v_mov_b32_e32 v111, v98
	v_mov_b32_e32 v112, v98
	v_mov_b32_e32 v113, v98
	v_mov_b32_e32 v54, v98
	v_mov_b32_e32 v55, v98
	v_mov_b32_e32 v56, v98
	v_mov_b32_e32 v57, v98
	v_mov_b32_e32 v78, v98
	v_mov_b32_e32 v79, v98
	v_mov_b32_e32 v80, v98
	v_mov_b32_e32 v81, v98
	v_mov_b32_e32 v62, v98
	v_mov_b32_e32 v63, v98
	v_mov_b32_e32 v64, v98
	v_mov_b32_e32 v65, v98
	v_mov_b32_e32 v86, v98
	v_mov_b32_e32 v87, v98
	v_mov_b32_e32 v88, v98
	v_mov_b32_e32 v89, v98
	v_mov_b32_e32 v70, v98
	v_mov_b32_e32 v71, v98
	v_mov_b32_e32 v72, v98
	v_mov_b32_e32 v73, v98
	v_mov_b32_e32 v94, v98
	v_mov_b32_e32 v95, v98
	v_mov_b32_e32 v96, v98
	v_mov_b32_e32 v97, v98
	v_mov_b32_e32 v114, v98
	v_mov_b32_e32 v115, v98
	v_mov_b32_e32 v116, v98
	v_mov_b32_e32 v117, v98
	v_mov_b32_e32 v118, v98
	v_mov_b32_e32 v119, v98
	v_mov_b32_e32 v120, v98
	v_mov_b32_e32 v121, v98
	v_mov_b32_e32 v2, v98
	v_mov_b32_e32 v3, v98
	v_mov_b32_e32 v4, v98
	v_mov_b32_e32 v5, v98
	v_mov_b32_e32 v14, v98
	v_mov_b32_e32 v15, v98
	v_mov_b32_e32 v16, v98
	v_mov_b32_e32 v17, v98
	v_mov_b32_e32 v6, v98
	v_mov_b32_e32 v7, v98
	v_mov_b32_e32 v8, v98
	v_mov_b32_e32 v9, v98
	v_mov_b32_e32 v18, v98
	v_mov_b32_e32 v19, v98
	v_mov_b32_e32 v20, v98
	v_mov_b32_e32 v21, v98
	v_mov_b32_e32 v10, v98
	v_mov_b32_e32 v11, v98
	v_mov_b32_e32 v12, v98
	v_mov_b32_e32 v13, v98
	v_mov_b32_e32 v22, v98
	v_mov_b32_e32 v23, v98
	v_mov_b32_e32 v24, v98
	v_mov_b32_e32 v25, v98
	v_mov_b32_e32 v122, v98
	v_mov_b32_e32 v123, v98
	v_mov_b32_e32 v124, v98
	v_mov_b32_e32 v125, v98
	v_mov_b32_e32 v126, v98
	v_mov_b32_e32 v127, v98
	v_mov_b32_e32 v128, v98
	v_mov_b32_e32 v129, v98
	v_mov_b32_e32 v26, v98
	v_mov_b32_e32 v27, v98
	v_mov_b32_e32 v28, v98
	v_mov_b32_e32 v29, v98
	v_mov_b32_e32 v38, v98
	v_mov_b32_e32 v39, v98
	v_mov_b32_e32 v40, v98
	v_mov_b32_e32 v41, v98
	v_mov_b32_e32 v30, v98
	v_mov_b32_e32 v31, v98
	v_mov_b32_e32 v32, v98
	v_mov_b32_e32 v33, v98
	v_mov_b32_e32 v42, v98
	v_mov_b32_e32 v43, v98
	v_mov_b32_e32 v44, v98
	v_mov_b32_e32 v45, v98
	v_mov_b32_e32 v34, v98
	v_mov_b32_e32 v35, v98
	v_mov_b32_e32 v36, v98
	v_mov_b32_e32 v37, v98
	v_mov_b32_e32 v46, v98
	v_mov_b32_e32 v47, v98
	v_mov_b32_e32 v48, v98
	v_mov_b32_e32 v49, v98
	v_readfirstlane_b32 s38, v0
	s_nop 3
	s_lshr_b32 s38, s38, 6
	s_cmp_ge_u32 s38, 4
	s_cbranch_scc1 .Lprio_P8
	s_setprio 1

.LBB0_1898:
	s_add_u32 s20, s20, 0x158080
	s_addc_u32 s21, s21, 0
	s_add_u32 s47, s22, 0x100
	v_mov_b32_e32 v2, 0
	s_addc_u32 s48, s23, 0
	s_mov_b32 s49, -2
	v_mov_b32_e32 v3, v2
	v_mov_b32_e32 v4, v2
	v_mov_b32_e32 v5, v2
	v_mov_b32_e32 v6, v2
	v_mov_b32_e32 v7, v2
	v_mov_b32_e32 v8, v2
	v_mov_b32_e32 v9, v2
	v_mov_b32_e32 v18, v2
	v_mov_b32_e32 v19, v2
	v_mov_b32_e32 v20, v2
	v_mov_b32_e32 v21, v2
	v_mov_b32_e32 v22, v2
	v_mov_b32_e32 v23, v2
	v_mov_b32_e32 v24, v2
	v_mov_b32_e32 v25, v2
	v_mov_b32_e32 v34, v2
	v_mov_b32_e32 v35, v2
	v_mov_b32_e32 v36, v2
	v_mov_b32_e32 v37, v2
	v_mov_b32_e32 v38, v2
	v_mov_b32_e32 v39, v2
	v_mov_b32_e32 v40, v2
	v_mov_b32_e32 v41, v2
	v_mov_b32_e32 v50, v2
	v_mov_b32_e32 v51, v2
	v_mov_b32_e32 v52, v2
	v_mov_b32_e32 v53, v2
	v_mov_b32_e32 v54, v2
	v_mov_b32_e32 v55, v2
	v_mov_b32_e32 v56, v2
	v_mov_b32_e32 v57, v2
	v_mov_b32_e32 v10, v2
	v_mov_b32_e32 v11, v2
	v_mov_b32_e32 v12, v2
	v_mov_b32_e32 v13, v2
	v_mov_b32_e32 v14, v2
	v_mov_b32_e32 v15, v2
	v_mov_b32_e32 v16, v2
	v_mov_b32_e32 v17, v2
	v_mov_b32_e32 v26, v2
	v_mov_b32_e32 v27, v2
	v_mov_b32_e32 v28, v2
	v_mov_b32_e32 v29, v2
	v_mov_b32_e32 v30, v2
	v_mov_b32_e32 v31, v2
	v_mov_b32_e32 v32, v2
	v_mov_b32_e32 v33, v2
	v_mov_b32_e32 v42, v2
	v_mov_b32_e32 v43, v2
	v_mov_b32_e32 v44, v2
	v_mov_b32_e32 v45, v2
	v_mov_b32_e32 v46, v2
	v_mov_b32_e32 v47, v2
	v_mov_b32_e32 v48, v2
	v_mov_b32_e32 v49, v2
	v_mov_b32_e32 v58, v2
	v_mov_b32_e32 v59, v2
	v_mov_b32_e32 v60, v2
	v_mov_b32_e32 v61, v2
	v_mov_b32_e32 v62, v2
	v_mov_b32_e32 v63, v2
	v_mov_b32_e32 v64, v2
	v_mov_b32_e32 v65, v2
	v_mov_b32_e32 v66, v2
	v_mov_b32_e32 v67, v2
	v_mov_b32_e32 v68, v2
	v_mov_b32_e32 v69, v2
	v_mov_b32_e32 v70, v2
	v_mov_b32_e32 v71, v2
	v_mov_b32_e32 v72, v2
	v_mov_b32_e32 v73, v2
	v_mov_b32_e32 v82, v2
	v_mov_b32_e32 v83, v2
	v_mov_b32_e32 v84, v2
	v_mov_b32_e32 v85, v2
	v_mov_b32_e32 v86, v2
	v_mov_b32_e32 v87, v2
	v_mov_b32_e32 v88, v2
	v_mov_b32_e32 v89, v2
	v_mov_b32_e32 v98, v2
	v_mov_b32_e32 v99, v2
	v_mov_b32_e32 v100, v2
	v_mov_b32_e32 v101, v2
	v_mov_b32_e32 v102, v2
	v_mov_b32_e32 v103, v2
	v_mov_b32_e32 v104, v2
	v_mov_b32_e32 v105, v2
	v_mov_b32_e32 v114, v2
	v_mov_b32_e32 v115, v2
	v_mov_b32_e32 v116, v2
	v_mov_b32_e32 v117, v2
	v_mov_b32_e32 v118, v2
	v_mov_b32_e32 v119, v2
	v_mov_b32_e32 v120, v2
	v_mov_b32_e32 v121, v2
	v_mov_b32_e32 v74, v2
	v_mov_b32_e32 v75, v2
	v_mov_b32_e32 v76, v2
	v_mov_b32_e32 v77, v2
	v_mov_b32_e32 v78, v2
	v_mov_b32_e32 v79, v2
	v_mov_b32_e32 v80, v2
	v_mov_b32_e32 v81, v2
	v_mov_b32_e32 v90, v2
	v_mov_b32_e32 v91, v2
	v_mov_b32_e32 v92, v2
	v_mov_b32_e32 v93, v2
	v_mov_b32_e32 v94, v2
	v_mov_b32_e32 v95, v2
	v_mov_b32_e32 v96, v2
	v_mov_b32_e32 v97, v2
	v_mov_b32_e32 v106, v2
	v_mov_b32_e32 v107, v2
	v_mov_b32_e32 v108, v2
	v_mov_b32_e32 v109, v2
	v_mov_b32_e32 v110, v2
	v_mov_b32_e32 v111, v2
	v_mov_b32_e32 v112, v2
	v_mov_b32_e32 v113, v2
	v_mov_b32_e32 v138, v2
	v_mov_b32_e32 v139, v2
	v_mov_b32_e32 v140, v2
	v_mov_b32_e32 v141, v2
	v_mov_b32_e32 v142, v2
	v_mov_b32_e32 v143, v2
	v_mov_b32_e32 v144, v2
	v_mov_b32_e32 v145, v2
	v_readfirstlane_b32 s22, v0
	s_nop 3
	s_lshr_b32 s22, s22, 6
	s_cmp_ge_u32 s22, 4
	s_cbranch_scc1 .Lprio_P10
	s_setprio 1
